# ssd_out<false>: the group's B and C tiles loaded once per item with coalesced loads and staged in LDS; each wave reads its 32 MFMA fragments from LDS instead of 32 scattered global loads
# speedup vs baseline: 1.0129x; 1.0096x over previous
.LBB0_1238:
	s_and_b32 s21, s54, 7
	s_lshl_b32 s0, s21, 3
	s_add_i32 s22, s0, s34
	s_lshl_b32 s14, s22, 6
	s_ashr_i32 s20, s54, 3
	s_ashr_i32 s15, s14, 31
	s_lshl_b32 s55, s20, 6
	s_lshl_b64 s[16:17], s[14:15], 1
	s_waitcnt vmcnt(8)
	v_or_b32_e32 v30, s55, v167
	v_lshl_add_u64 v[28:29], v[158:159], 0, s[16:17]
	v_mad_i64_i32 v[0:1], s[0:1], v30, s77, v[28:29]
	v_or_b32_e32 v4, 8, v30
	global_load_dwordx4 v[0:3], v[0:1], off
	v_mad_i64_i32 v[4:5], s[0:1], v4, s77, v[28:29]
	v_or_b32_e32 v8, 16, v30
	global_load_dwordx4 v[4:7], v[4:5], off
	v_mad_i64_i32 v[8:9], s[0:1], v8, s77, v[28:29]
	v_or_b32_e32 v12, 24, v30
	global_load_dwordx4 v[8:11], v[8:9], off
	v_mad_i64_i32 v[12:13], s[0:1], v12, s77, v[28:29]
	v_or_b32_e32 v16, 32, v30
	global_load_dwordx4 v[12:15], v[12:13], off
	v_mad_i64_i32 v[16:17], s[0:1], v16, s77, v[28:29]
	v_or_b32_e32 v20, 40, v30
	global_load_dwordx4 v[16:19], v[16:17], off
	v_mad_i64_i32 v[20:21], s[0:1], v20, s77, v[28:29]
	v_or_b32_e32 v24, 48, v30
	global_load_dwordx4 v[20:23], v[20:21], off
	v_mad_i64_i32 v[24:25], s[0:1], v24, s77, v[28:29]
	v_or_b32_e32 v30, 56, v30
	global_load_dwordx4 v[24:27], v[24:25], off
	v_mad_i64_i32 v[28:29], s[0:1], v30, s77, v[28:29]
	global_load_dwordx4 v[28:31], v[28:29], off
	s_lshl_b32 s0, s20, 6
	s_add_i32 s0, s0, s22
	s_lshl_b32 s0, s0, 9
	v_lshl_add_u32 v198, v161, 3, s0
	v_mov_b32_e32 v199, 0
	v_lshl_add_u64 v[198:199], s[24:25], 0, v[198:199]
	s_mov_b64 s[0:1], 0x400000
	s_nop 0
	v_lshl_add_u64 v[198:199], v[198:199], 0, s[0:1]
	global_load_dwordx2 v[198:199], v[198:199], off
	v_lshrrev_b32_e32 v239, 4, v219
	v_and_b32_e32 v240, 15, v219
	v_mul_u32_u24_e32 v241, 0x110, v239
	v_lshl_add_u32 v241, v240, 4, v241
	v_add_u32_e32 v241, 0x16000, v241
	v_add_u32_e32 v239, s55, v239
	v_mul_u32_u24_e32 v239, 0x3000, v239
	v_lshl_add_u32 v239, v240, 4, v239
	v_lshl_add_u32 v239, s21, 8, v239
	v_add_u32_e32 v240, 0x2800, v239
	global_load_dwordx4 v[82:85], v240, s[8:9]
	v_add_u32_e32 v240, 0x62800, v239
	global_load_dwordx4 v[92:95], v240, s[8:9]
	v_add_u32_e32 v240, 0x2000, v239
	global_load_dwordx4 v[96:99], v240, s[8:9]
	v_add_u32_e32 v240, 0x62000, v239
	global_load_dwordx4 v[104:107], v240, s[8:9]
	s_ashr_i32 s23, s22, 31
	s_lshl_b64 s[18:19], s[22:23], 2
	s_add_u32 s0, s26, s18
	s_addc_u32 s1, s27, s19
	v_or_b32_e32 v174, s55, v166
	v_lshlrev_b32_e32 v32, 1, v160
	s_movk_i32 s56, 0x2000
	v_mov_b32_e32 v173, v33
	s_waitcnt vmcnt(12)
	ds_write_b128 v213, v[0:3]
	s_waitcnt vmcnt(11)
	ds_write_b128 v213, v[4:7] offset:1280
	s_waitcnt vmcnt(10)
	ds_write_b128 v213, v[8:11] offset:2560
	s_waitcnt vmcnt(9)
	ds_write_b128 v213, v[12:15] offset:3840
	s_waitcnt vmcnt(8)
	ds_write_b128 v213, v[16:19] offset:5120
	s_waitcnt vmcnt(7)
	ds_write_b128 v213, v[20:23] offset:6400
	s_waitcnt vmcnt(6)
	ds_write_b128 v213, v[24:27] offset:7680
	s_waitcnt vmcnt(5)
	ds_write_b128 v213, v[28:31] offset:8960
	s_lshl_b32 s86, s21, 8
	s_ashr_i32 s21, s20, 31
	s_waitcnt vmcnt(4)
	ds_write_b32 v190, v198
	ds_write_b32 v191, v199
	s_waitcnt vmcnt(3)
	ds_write_b128 v241, v[82:85]
	s_waitcnt vmcnt(2)
	ds_write_b128 v241, v[92:95] offset:8704
	s_waitcnt vmcnt(1)
	ds_write_b128 v241, v[96:99] offset:17408
	s_waitcnt vmcnt(0)
	ds_write_b128 v241, v[104:107] offset:26112
	v_lshrrev_b32_e32 v238, 4, v219
	v_and_b32_e32 v238, 3, v238
	v_mul_u32_u24_e32 v237, 0x110, v166
	v_lshl_add_u32 v237, v238, 4, v237
	v_add_u32_e32 v237, 0x16000, v237
	v_add_u32_e32 v238, 0x4400, v237
	s_waitcnt lgkmcnt(0)
	s_barrier
	v_mov_b64_e32 v[0:1], s[8:9]
	v_mad_i64_i32 v[0:1], s[0:1], v174, s77, v[0:1]
	v_lshl_add_u64 v[0:1], v[0:1], 0, s[86:87]
	v_lshl_add_u64 v[8:9], v[0:1], 0, v[32:33]
	s_mov_b64 s[0:1], 0x2800
	v_lshl_add_u64 v[74:75], v[8:9], 0, s[0:1]
	v_add_co_u32_e64 v0, s[0:1], s56, v8
	s_movk_i32 s77, 0x3000
	s_nop 0
	v_addc_co_u32_e64 v1, s[0:1], 0, v9, s[0:1]
	s_mov_b32 s0, 0x32000
	s_nop 0
	v_add_co_u32_e64 v30, s[0:1], s0, v8
	ds_read_b128 v[4:7], v237
	s_nop 0
	ds_read_b128 v[0:3], v237 offset:64
	ds_read_b128 v[70:73], v237 offset:128
	ds_read_b128 v[66:69], v237 offset:192
	v_addc_co_u32_e64 v31, s[0:1], 0, v9, s[0:1]
	s_mov_b32 s0, 0x62000
	s_nop 0
	v_add_co_u32_e64 v88, s[0:1], s0, v8
	ds_read_b128 v[62:65], v237 offset:4352
	ds_read_b128 v[58:61], v237 offset:4416
	ds_read_b128 v[54:57], v237 offset:4480
	ds_read_b128 v[50:53], v237 offset:4544
	v_addc_co_u32_e64 v89, s[0:1], 0, v9, s[0:1]
	s_mov_b32 s0, 0x92000
	s_nop 0
	v_add_co_u32_e64 v86, s[0:1], s0, v8
	ds_read_b128 v[46:49], v237 offset:8704
	ds_read_b128 v[42:45], v237 offset:8768
	ds_read_b128 v[38:41], v237 offset:8832
	ds_read_b128 v[24:27], v237 offset:8896
	v_addc_co_u32_e64 v87, s[0:1], 0, v9, s[0:1]
	ds_read_b128 v[20:23], v237 offset:13056
	ds_read_b128 v[16:19], v237 offset:13120
	ds_read_b128 v[8:11], v237 offset:13184
	ds_read_b128 v[12:15], v237 offset:13248
	s_waitcnt lgkmcnt(0)
	ds_read2_b32 v[102:103], v192 offset1:16
	ds_read2_b32 v[28:29], v192 offset0:32 offset1:48
	ds_read_b128 v[82:85], v238
	ds_read_b128 v[92:95], v238 offset:64
	ds_read_b128 v[96:99], v238 offset:128
	ds_read_b128 v[104:107], v238 offset:192
	s_waitcnt lgkmcnt(0)
	s_lshl_b32 s0, s20, 12
	s_lshl_b32 s1, s22, 6
	s_add_i32 s0, s0, s1
	v_or_b32_e32 v200, s0, v166
	v_mov_b32_e32 v201, 0
	v_lshlrev_b64 v[200:201], 8, v[200:201]
	v_lshl_add_u64 v[200:201], v[164:165], 0, v[200:201]
	global_load_dwordx4 v[144:147], v[200:201], off
	global_load_dwordx4 v[148:151], v[200:201], off offset:64
	global_load_dwordx4 v[152:155], v[200:201], off offset:128
	global_load_dwordx4 v[222:225], v[200:201], off offset:192
	v_mfma_f32_16x16x32_bf16 v[74:77], v[82:85], v[4:7], 0
	ds_read_b64 v[100:101], v193
	ds_read_b32 v32, v195
	ds_read_b32 v90, v196
	ds_read_b32 v118, v197
	ds_read_b32 v91, v208
	s_mov_b32 s0, 0x5040100
	v_mfma_f32_16x16x32_bf16 v[74:77], v[92:95], v[0:3], v[74:77]
	v_mfma_f32_16x16x32_bf16 v[74:77], v[96:99], v[70:73], v[74:77]
	v_mfma_f32_16x16x32_bf16 v[108:111], v[82:85], v[62:65], 0
	v_mfma_f32_16x16x32_bf16 v[78:81], v[104:107], v[66:69], v[74:77]
	s_waitcnt lgkmcnt(4)
	s_nop 3
	s_nop 0
	v_sub_f32_e32 v76, v103, v100
	v_min_f32_e32 v76, 0, v76
	v_mfma_f32_16x16x32_bf16 v[108:111], v[92:95], v[58:61], v[108:111]
	v_mul_f32_e32 v76, 0x3fb8aa3b, v76
	v_exp_f32_e32 v114, v76
	v_sub_f32_e32 v76, v103, v101
	v_min_f32_e32 v76, 0, v76
	v_mul_f32_e32 v76, 0x3fb8aa3b, v76
	v_mfma_f32_16x16x32_bf16 v[108:111], v[96:99], v[54:57], v[108:111]
	v_exp_f32_e32 v115, v76
	s_waitcnt lgkmcnt(3)
	v_sub_f32_e32 v76, v103, v32
	s_waitcnt lgkmcnt(1)
	v_sub_f32_e32 v77, v103, v118
	v_min_f32_e32 v76, 0, v76
	v_min_f32_e32 v77, 0, v77
	v_mul_f32_e32 v76, 0x3fb8aa3b, v76
	v_mul_f32_e32 v77, 0x3fb8aa3b, v77
	v_exp_f32_e32 v76, v76
	v_exp_f32_e32 v77, v77
	v_mfma_f32_16x16x32_bf16 v[108:111], v[104:107], v[50:53], v[108:111]
	v_sub_f32_e32 v74, v102, v100
	v_min_f32_e32 v74, 0, v74
	v_mul_f32_e32 v74, 0x3fb8aa3b, v74
	s_waitcnt lgkmcnt(0)
	v_pk_mul_f32 v[76:77], v[90:91], v[76:77]
	v_exp_f32_e32 v119, v74
	v_sub_f32_e32 v74, v102, v101
	s_nop 0
	v_pk_mul_f32 v[76:77], v[76:77], v[110:111]
	v_mfma_f32_16x16x32_bf16 v[110:113], v[82:85], v[46:49], 0
	v_min_f32_e32 v74, 0, v74
	v_mul_f32_e32 v74, 0x3fb8aa3b, v74
	v_exp_f32_e32 v120, v74
	v_mfma_f32_16x16x32_bf16 v[82:85], v[82:85], v[20:23], 0
	v_sub_f32_e32 v74, v102, v32
	v_sub_f32_e32 v75, v102, v118
	v_min_f32_e32 v74, 0, v74
	v_min_f32_e32 v75, 0, v75
	v_mfma_f32_16x16x32_bf16 v[82:85], v[92:95], v[16:19], v[82:85]
	v_mul_f32_e32 v74, 0x3fb8aa3b, v74
	v_mul_f32_e32 v75, 0x3fb8aa3b, v75
	v_exp_f32_e32 v74, v74
	v_exp_f32_e32 v75, v75
	v_mfma_f32_16x16x32_bf16 v[82:85], v[96:99], v[8:11], v[82:85]
	v_mul_f32_e64 v74, v90, v74
	v_mul_f32_e64 v75, v91, v75
	v_mfma_f32_16x16x32_bf16 v[110:113], v[92:95], v[42:45], v[110:113]
	v_mul_f32_e64 v74, v74, v80
	v_mul_f32_e64 v75, v75, v81
	v_sub_f32_e32 v80, v28, v100
	v_min_f32_e32 v80, 0, v80
	v_mfma_f32_16x16x32_bf16 v[92:95], v[104:107], v[12:15], v[82:85]
	v_mul_f32_e32 v80, 0x3fb8aa3b, v80
	v_exp_f32_e32 v116, v80
	v_sub_f32_e32 v80, v28, v101
	v_sub_f32_e32 v82, v29, v100
	v_sub_f32_e32 v83, v29, v101
	v_min_f32_e32 v82, 0, v82
	v_min_f32_e32 v83, 0, v83
	v_mfma_f32_16x16x32_bf16 v[110:113], v[96:99], v[38:41], v[110:113]
	v_mul_f32_e32 v82, 0x3fb8aa3b, v82
	v_mul_f32_e32 v83, 0x3fb8aa3b, v83
	ds_read_b64 v[96:97], v194
	v_min_f32_e32 v80, 0, v80
	v_exp_f32_e32 v82, v82
	v_exp_f32_e32 v83, v83
	v_mul_f32_e32 v80, 0x3fb8aa3b, v80
	v_exp_f32_e32 v117, v80
	v_sub_f32_e32 v80, v28, v32
	v_sub_f32_e32 v32, v29, v32
	v_min_f32_e32 v32, 0, v32
	s_waitcnt lgkmcnt(0)
	v_pk_mul_f32 v[82:83], v[96:97], v[82:83]
	v_mul_f32_e32 v32, 0x3fb8aa3b, v32
	v_sub_f32_e32 v81, v28, v118
	v_pk_mul_f32 v[82:83], v[82:83], v[92:93]
	v_exp_f32_e32 v92, v32
	v_sub_f32_e32 v32, v29, v118
	v_min_f32_e32 v80, 0, v80
	v_min_f32_e32 v81, 0, v81
	v_min_f32_e32 v32, 0, v32
	v_mul_f32_e32 v80, 0x3fb8aa3b, v80
	v_mul_f32_e32 v81, 0x3fb8aa3b, v81
	v_mul_f32_e32 v84, v96, v119
	v_mul_f32_e32 v32, 0x3fb8aa3b, v32
	v_exp_f32_e32 v80, v80
	v_exp_f32_e32 v81, v81
	v_mul_f32_e32 v78, v84, v78
	v_exp_f32_e32 v93, v32
	v_mfma_f32_16x16x32_bf16 v[110:113], v[104:107], v[24:27], v[110:113]
	v_cndmask_b32_e64 v126, v78, 0, s[46:47]
	v_mul_f32_e32 v78, v97, v120
	v_mul_f32_e32 v78, v78, v79
	v_cndmask_b32_e64 v127, 0, v78, s[48:49]
	v_pk_mul_f32 v[78:79], v[96:97], v[114:115]
	v_pk_mul_f32 v[80:81], v[90:91], v[80:81]
	v_pk_mul_f32 v[84:85], v[78:79], v[108:109]
	v_pk_mul_f32 v[78:79], v[96:97], v[116:117]
	v_pk_mul_f32 v[90:91], v[90:91], v[92:93]
	v_pk_mul_f32 v[78:79], v[78:79], v[110:111]
	v_pk_mul_f32 v[90:91], v[90:91], v[94:95]
	ds_read_b128 v[92:95], v238 offset:4352
	ds_read_b128 v[96:99], v238 offset:4416
	ds_read_b128 v[104:107], v238 offset:4480
	ds_read_b128 v[108:111], v238 offset:4544
	s_waitcnt lgkmcnt(0)
	v_pk_mul_f32 v[80:81], v[80:81], v[112:113]
	ds_read_b128 v[112:115], v193 offset:64
	v_mfma_f32_16x16x32_bf16 v[116:119], v[92:95], v[62:65], 0
	s_waitcnt lgkmcnt(0)
	v_sub_f32_e32 v30, v103, v112
	v_min_f32_e32 v30, 0, v30
	v_mul_f32_e32 v30, 0x3fb8aa3b, v30
	v_mfma_f32_16x16x32_bf16 v[120:123], v[92:95], v[46:49], 0
	v_exp_f32_e32 v32, v30
	v_sub_f32_e32 v30, v103, v113
	v_min_f32_e32 v30, 0, v30
	v_mfma_f32_16x16x32_bf16 v[92:95], v[92:95], v[20:23], 0
	v_mul_f32_e32 v30, 0x3fb8aa3b, v30
	v_exp_f32_e32 v128, v30
	v_sub_f32_e32 v100, v28, v112
	v_mfma_f32_16x16x32_bf16 v[116:119], v[96:99], v[58:61], v[116:119]
	v_sub_f32_e32 v101, v28, v113
	v_min_f32_e32 v100, 0, v100
	v_min_f32_e32 v101, 0, v101
	v_mfma_f32_16x16x32_bf16 v[120:123], v[96:99], v[42:45], v[120:123]
	v_mul_f32_e32 v100, 0x3fb8aa3b, v100
	v_mul_f32_e32 v101, 0x3fb8aa3b, v101
	v_exp_f32_e32 v100, v100
	v_mfma_f32_16x16x32_bf16 v[92:95], v[96:99], v[16:19], v[92:95]
	v_sub_f32_e32 v96, v29, v112
	v_min_f32_e32 v96, 0, v96
	v_mul_f32_e32 v96, 0x3fb8aa3b, v96
	v_mfma_f32_16x16x32_bf16 v[116:119], v[104:107], v[54:57], v[116:119]
	v_exp_f32_e32 v101, v101
	v_sub_f32_e32 v30, v103, v114
	v_sub_f32_e32 v31, v103, v115
	v_mfma_f32_16x16x32_bf16 v[120:123], v[104:107], v[38:41], v[120:123]
	v_min_f32_e32 v30, 0, v30
	v_min_f32_e32 v31, 0, v31
	v_sub_f32_e32 v124, v28, v114
	v_mfma_f32_16x16x32_bf16 v[92:95], v[104:107], v[8:11], v[92:95]
	v_exp_f32_e32 v104, v96
	v_sub_f32_e32 v96, v29, v113
	v_min_f32_e32 v96, 0, v96
	v_mul_f32_e32 v96, 0x3fb8aa3b, v96
	v_exp_f32_e32 v105, v96
	ds_read_b128 v[96:99], v194 offset:64
	v_mfma_f32_16x16x32_bf16 v[116:119], v[108:111], v[50:53], v[116:119]
	v_sub_f32_e32 v125, v28, v115
	v_mul_f32_e32 v30, 0x3fb8aa3b, v30
	v_mul_f32_e32 v31, 0x3fb8aa3b, v31
	s_waitcnt lgkmcnt(0)
	v_mul_f32_e32 v32, v96, v32
	v_mfma_f32_16x16x32_bf16 v[120:123], v[108:111], v[24:27], v[120:123]
	s_nop 1
	v_mul_f32_e32 v32, v32, v116
	v_pk_mul_f32 v[100:101], v[96:97], v[100:101]
	v_min_f32_e32 v124, 0, v124
	v_mfma_f32_16x16x32_bf16 v[92:95], v[108:111], v[12:15], v[92:95]
	v_cndmask_b32_e64 v108, v32, 0, s[46:47]
	v_mul_f32_e32 v32, v97, v128
	v_mul_f32_e32 v32, v32, v117
	v_cndmask_b32_e64 v109, 0, v32, s[48:49]
	v_sub_f32_e32 v32, v29, v114
	v_min_f32_e32 v32, 0, v32
	v_pk_mul_f32 v[96:97], v[96:97], v[104:105]
	v_mul_f32_e32 v32, 0x3fb8aa3b, v32
	v_min_f32_e32 v125, 0, v125
	v_pk_mul_f32 v[92:93], v[96:97], v[92:93]
	v_exp_f32_e32 v96, v32
	v_sub_f32_e32 v32, v29, v115
	v_exp_f32_e32 v30, v30
	v_exp_f32_e32 v31, v31
	v_mul_f32_e32 v124, 0x3fb8aa3b, v124
	v_mul_f32_e32 v125, 0x3fb8aa3b, v125
	v_min_f32_e32 v32, 0, v32
	v_exp_f32_e32 v124, v124
	v_exp_f32_e32 v125, v125
	v_mul_f32_e32 v32, 0x3fb8aa3b, v32
	v_exp_f32_e32 v97, v32
	v_pk_mul_f32 v[30:31], v[98:99], v[30:31]
	v_pk_mul_f32 v[100:101], v[100:101], v[120:121]
	v_pk_mul_f32 v[104:105], v[30:31], v[118:119]
	v_pk_mul_f32 v[30:31], v[98:99], v[124:125]
	v_cvt_pk_bf16_f32 v78, v78, v79
	v_pk_mul_f32 v[106:107], v[30:31], v[122:123]
	v_pk_mul_f32 v[30:31], v[98:99], v[96:97]
	v_cvt_pk_bf16_f32 v79, v80, v81
	v_pk_mul_f32 v[94:95], v[30:31], v[94:95]
	v_cvt_pk_bf16_f32 v31, v74, v75
	v_cvt_pk_bf16_f32 v75, v76, v77
	v_cvt_pk_bf16_f32 v77, v104, v105
	v_cvt_pk_bf16_f32 v74, v84, v85
	v_cndmask_b32_e64 v84, v77, 0, s[52:53]
	v_lshrrev_b32_e32 v77, 16, v77
	v_cndmask_b32_e64 v77, v77, 0, s[50:51]
	v_perm_b32 v77, v77, v84, s0
	v_cvt_pk_bf16_f32 v80, v100, v101
	v_cvt_pk_bf16_f32 v81, v106, v107
	v_cvt_pk_bf16_f32 v82, v82, v83
	v_cvt_pk_bf16_f32 v83, v90, v91
	v_cvt_pk_bf16_f32 v84, v92, v93
	v_cvt_pk_bf16_f32 v85, v94, v95
	ds_read_b128 v[90:93], v238 offset:8704
	ds_read_b128 v[94:97], v238 offset:8768
	ds_read_b128 v[98:101], v238 offset:8832
	ds_read_b128 v[104:107], v238 offset:8896
	s_waitcnt lgkmcnt(0)
	v_cvt_pk_bf16_f32 v76, v108, v109
	ds_read_b128 v[108:111], v193 offset:128
	v_mfma_f32_16x16x32_bf16 v[112:115], v[90:93], v[46:49], 0
	s_waitcnt lgkmcnt(0)
	v_sub_f32_e32 v88, v28, v108
	v_min_f32_e32 v88, 0, v88
	v_mul_f32_e32 v88, 0x3fb8aa3b, v88
	v_exp_f32_e32 v118, v88
	v_sub_f32_e32 v88, v28, v109
	v_min_f32_e32 v88, 0, v88
	v_mul_f32_e32 v88, 0x3fb8aa3b, v88
	v_exp_f32_e32 v119, v88
	v_sub_f32_e32 v88, v28, v110
	v_min_f32_e32 v88, 0, v88
	v_mul_f32_e32 v88, 0x3fb8aa3b, v88
	v_exp_f32_e32 v116, v88
	v_sub_f32_e32 v88, v28, v111
	v_min_f32_e32 v88, 0, v88
	v_mul_f32_e32 v88, 0x3fb8aa3b, v88
	v_exp_f32_e32 v117, v88
	v_mfma_f32_16x16x32_bf16 v[88:91], v[90:93], v[20:23], 0
	v_cndmask_b32_e64 v32, v31, 0, s[52:53]
	v_lshrrev_b32_e32 v31, 16, v31
	v_cndmask_b32_e64 v31, v31, 0, s[50:51]
	v_mfma_f32_16x16x32_bf16 v[88:91], v[94:97], v[16:19], v[88:91]
	v_perm_b32 v31, v31, v32, s0
	v_cvt_pk_bf16_f32 v30, v126, v127
	v_mul_f32_e32 v28, 0x3fb8aa3b, v28
	v_mfma_f32_16x16x32_bf16 v[88:91], v[98:101], v[8:11], v[88:91]
	v_exp_f32_e32 v178, v28
	v_mul_f32_e32 v28, 0x3fb8aa3b, v29
	v_exp_f32_e32 v28, v28
	v_mfma_f32_16x16x32_bf16 v[90:93], v[104:107], v[12:15], v[88:91]
	v_mov_b32_e32 v32, v33
	s_nop 1
	s_nop 0
	v_sub_f32_e32 v88, v29, v108
	v_sub_f32_e32 v89, v29, v109
	v_mfma_f32_16x16x32_bf16 v[112:115], v[94:97], v[42:45], v[112:115]
	v_min_f32_e32 v88, 0, v88
	v_min_f32_e32 v89, 0, v89
	v_mul_f32_e32 v88, 0x3fb8aa3b, v88
	v_mul_f32_e32 v89, 0x3fb8aa3b, v89
	ds_read_b128 v[94:97], v194 offset:128
	v_exp_f32_e32 v88, v88
	v_exp_f32_e32 v89, v89
	v_mfma_f32_16x16x32_bf16 v[112:115], v[98:101], v[38:41], v[112:115]
	s_waitcnt lgkmcnt(0)
	v_mul_f32_e32 v98, v94, v118
	v_pk_mul_f32 v[88:89], v[94:95], v[88:89]
	v_mfma_f32_16x16x32_bf16 v[112:115], v[104:107], v[24:27], v[112:115]
	v_mul_f32_e64 v90, v88, v90
	v_mul_f32_e64 v91, v89, v91
	v_sub_f32_e32 v88, v29, v110
	v_min_f32_e32 v88, 0, v88
	v_mul_f32_e32 v88, 0x3fb8aa3b, v88
	v_exp_f32_e32 v94, v88
	v_sub_f32_e32 v88, v29, v111
	v_min_f32_e32 v88, 0, v88
	v_mul_f32_e32 v98, v98, v112
	v_mul_f32_e32 v88, 0x3fb8aa3b, v88
	v_cndmask_b32_e64 v120, v98, 0, s[46:47]
	v_mul_f32_e32 v98, v95, v119
	v_exp_f32_e32 v95, v88
	v_mul_f32_e32 v98, v98, v113
	v_cndmask_b32_e64 v121, 0, v98, s[48:49]
	v_pk_mul_f32 v[88:89], v[96:97], v[116:117]
	v_pk_mul_f32 v[94:95], v[96:97], v[94:95]
	v_pk_mul_f32 v[88:89], v[88:89], v[114:115]
	v_pk_mul_f32 v[92:93], v[94:95], v[92:93]
	ds_read_b128 v[94:97], v238 offset:13056
	ds_read_b128 v[98:101], v238 offset:13120
	ds_read_b128 v[104:107], v238 offset:13184
	ds_read_b128 v[108:111], v238 offset:13248
	s_waitcnt lgkmcnt(0)
	v_mfma_f32_16x16x32_bf16 v[94:97], v[94:97], v[20:23], 0
	ds_read_b128 v[112:115], v193 offset:192
	ds_read_b128 v[116:119], v194 offset:192
	v_cvt_pk_bf16_f32 v90, v90, v91
	v_cvt_pk_bf16_f32 v91, v92, v93
	v_mfma_f32_16x16x32_bf16 v[94:97], v[98:101], v[16:19], v[94:97]
	s_waitcnt lgkmcnt(1)
	v_sub_f32_e32 v86, v29, v112
	v_min_f32_e32 v86, 0, v86
	v_mul_f32_e32 v86, 0x3fb8aa3b, v86
	v_mfma_f32_16x16x32_bf16 v[94:97], v[104:107], v[8:11], v[94:97]
	v_exp_f32_e32 v86, v86
	v_sub_f32_e32 v87, v29, v115
	v_min_f32_e32 v87, 0, v87
	v_mfma_f32_16x16x32_bf16 v[94:97], v[108:111], v[12:15], v[94:97]
	s_waitcnt lgkmcnt(0)
	v_mul_f32_e32 v86, v116, v86
	v_mul_f32_e32 v87, 0x3fb8aa3b, v87
	v_exp_f32_e32 v87, v87
	s_nop 3
	v_mul_f32_e32 v86, v86, v94
	v_cndmask_b32_e64 v98, v86, 0, s[46:47]
	v_sub_f32_e32 v86, v29, v113
	v_min_f32_e32 v86, 0, v86
	v_mul_f32_e32 v86, 0x3fb8aa3b, v86
	v_exp_f32_e32 v86, v86
	s_nop 0
	v_mul_f32_e32 v86, v117, v86
	v_mul_f32_e32 v86, v86, v95
	v_cndmask_b32_e64 v99, 0, v86, s[48:49]
	v_sub_f32_e32 v86, v29, v114
	v_min_f32_e32 v86, 0, v86
	v_mul_f32_e32 v86, 0x3fb8aa3b, v86
	v_exp_f32_e32 v86, v86
	v_cvt_pk_bf16_f32 v92, v98, v99
	v_mul_f32_e32 v98, 0x3fb8aa3b, v102
	v_mul_f32_e32 v102, 0x3fb8aa3b, v103
	v_pk_mul_f32 v[86:87], v[118:119], v[86:87]
	v_exp_f32_e32 v180, v98
	v_pk_mul_f32 v[94:95], v[86:87], v[96:97]
	v_cvt_pk_bf16_f32 v87, v88, v89
	v_cvt_pk_bf16_f32 v93, v94, v95
	v_cndmask_b32_e64 v88, v87, 0, s[52:53]
	v_lshrrev_b32_e32 v87, 16, v87
	v_cndmask_b32_e64 v94, v93, 0, s[52:53]
	v_lshrrev_b32_e32 v93, 16, v93
	v_cndmask_b32_e64 v87, v87, 0, s[50:51]
	v_cndmask_b32_e64 v93, v93, 0, s[50:51]
	v_perm_b32 v87, v87, v88, s0
	v_perm_b32 v93, v93, v94, s0
	s_lshl_b64 s[0:1], s[20:21], 12
	s_lshl_b64 s[20:21], s[22:23], 6
	s_add_u32 s0, s20, s0
	s_addc_u32 s1, s21, s1
	v_mov_b32_e32 v95, s1
	v_or_b32_e32 v94, s0, v166
	v_lshlrev_b64 v[94:95], 8, v[94:95]
	v_lshl_add_u64 v[142:143], v[164:165], 0, v[94:95]
	v_cvt_pk_bf16_f32 v86, v120, v121
	s_waitcnt vmcnt(3)
	v_mfma_f32_16x16x32_bf16 v[94:97], v[144:147], v[4:7], 0
	v_exp_f32_e32 v176, v102
	s_movk_i32 s0, 0x1000
	v_mfma_f32_16x16x32_bf16 v[98:101], v[144:147], v[62:65], 0
	v_mov_b32_e32 v88, v33
	v_mov_b32_e32 v89, v33
	v_mfma_f32_16x16x32_bf16 v[102:105], v[144:147], v[46:49], 0
	v_mfma_f32_16x16x32_bf16 v[106:109], v[144:147], v[20:23], 0
	s_waitcnt vmcnt(2)
	v_mfma_f32_16x16x32_bf16 v[94:97], v[148:151], v[0:3], v[94:97]
	v_mfma_f32_16x16x32_bf16 v[98:101], v[148:151], v[58:61], v[98:101]
	v_mfma_f32_16x16x32_bf16 v[102:105], v[148:151], v[42:45], v[102:105]
	v_mfma_f32_16x16x32_bf16 v[106:109], v[148:151], v[16:19], v[106:109]
	v_add_co_u32_e64 v110, s[0:1], s0, v142
	s_nop 1
	v_addc_co_u32_e64 v111, s[0:1], 0, v143, s[0:1]
	v_add_co_u32_e64 v126, s[0:1], s56, v142
	s_waitcnt vmcnt(1)
	v_mfma_f32_16x16x32_bf16 v[94:97], v[152:155], v[70:73], v[94:97]
	v_addc_co_u32_e64 v127, s[0:1], 0, v143, s[0:1]
	global_load_dwordx4 v[122:125], v[126:127], off offset:-4096
	global_load_dwordx4 v[128:131], v[110:111], off offset:64
	global_load_dwordx4 v[132:135], v[110:111], off offset:128
	global_load_dwordx4 v[136:139], v[110:111], off offset:192
	v_mfma_f32_16x16x32_bf16 v[98:101], v[152:155], v[54:57], v[98:101]
	v_mfma_f32_16x16x32_bf16 v[102:105], v[152:155], v[38:41], v[102:105]
	v_mfma_f32_16x16x32_bf16 v[106:109], v[152:155], v[8:11], v[106:109]
	s_waitcnt vmcnt(4)
	v_mfma_f32_16x16x32_bf16 v[94:97], v[222:225], v[66:69], v[94:97]
	v_mfma_f32_16x16x32_bf16 v[98:101], v[222:225], v[50:53], v[98:101]
	v_mfma_f32_16x16x32_bf16 v[102:105], v[222:225], v[24:27], v[102:105]
	s_nop 5
	v_mul_f32_e64 v96, v180, v96
	v_mul_f32_e64 v97, v180, v97
	v_pk_mul_f32 v[94:95], v[180:181], v[94:95] op_sel_hi:[0,1]
	v_mfma_f32_16x16x32_bf16 v[106:109], v[222:225], v[12:15], v[106:109]
	s_waitcnt vmcnt(3)
	v_mfma_f32_16x16x32_bf16 v[110:113], v[122:125], v[4:7], 0
	v_mul_f32_e64 v104, v178, v104
	v_mul_f32_e64 v105, v178, v105
	v_pk_mul_f32 v[102:103], v[178:179], v[102:103] op_sel_hi:[0,1]
	s_nop 2
	v_pk_mul_f32 v[108:109], v[28:29], v[108:109] op_sel_hi:[0,1]
	v_mfma_f32_16x16x32_bf16 v[114:117], v[122:125], v[62:65], 0
	v_mul_f32_e64 v106, v28, v106
	v_mul_f32_e64 v107, v28, v107
	v_mfma_f32_16x16x32_bf16 v[118:121], v[122:125], v[46:49], 0
	v_mfma_f32_16x16x32_bf16 v[122:125], v[122:125], v[20:23], 0
	s_waitcnt vmcnt(2)
	v_mfma_f32_16x16x32_bf16 v[110:113], v[128:131], v[0:3], v[110:113]
	v_mfma_f32_16x16x32_bf16 v[114:117], v[128:131], v[58:61], v[114:117]
	v_mfma_f32_16x16x32_bf16 v[118:121], v[128:131], v[42:45], v[118:121]
	v_mfma_f32_16x16x32_bf16 v[122:125], v[128:131], v[16:19], v[122:125]
	s_waitcnt vmcnt(1)
	v_mfma_f32_16x16x32_bf16 v[110:113], v[132:135], v[70:73], v[110:113]
	v_mfma_f32_16x16x32_bf16 v[114:117], v[132:135], v[54:57], v[114:117]
	v_mfma_f32_16x16x32_bf16 v[118:121], v[132:135], v[38:41], v[118:121]
	v_mfma_f32_16x16x32_bf16 v[122:125], v[132:135], v[8:11], v[122:125]
	s_waitcnt vmcnt(0)
	v_mfma_f32_16x16x32_bf16 v[110:113], v[136:139], v[66:69], v[110:113]
	v_mfma_f32_16x16x32_bf16 v[114:117], v[136:139], v[50:53], v[114:117]
	v_mfma_f32_16x16x32_bf16 v[118:121], v[136:139], v[24:27], v[118:121]
	s_nop 5
	v_mul_f32_e64 v112, v180, v112
	v_mul_f32_e64 v113, v180, v113
	v_pk_mul_f32 v[110:111], v[180:181], v[110:111] op_sel_hi:[0,1]
	v_pk_mul_f32 v[116:117], v[176:177], v[116:117] op_sel_hi:[0,1]
	v_mfma_f32_16x16x32_bf16 v[122:125], v[136:139], v[12:15], v[122:125]
	global_load_dwordx4 v[138:141], v[126:127], off
	global_load_dwordx4 v[144:147], v[126:127], off offset:64
	global_load_dwordx4 v[148:151], v[126:127], off offset:128
	global_load_dwordx4 v[152:155], v[126:127], off offset:192
	v_pk_mul_f32 v[114:115], v[176:177], v[114:115] op_sel_hi:[0,1]
	s_waitcnt vmcnt(3)
	v_mfma_f32_16x16x32_bf16 v[126:129], v[138:141], v[4:7], 0
	v_mul_f32_e64 v120, v178, v120
	v_mul_f32_e64 v121, v178, v121
	v_pk_mul_f32 v[118:119], v[178:179], v[118:119] op_sel_hi:[0,1]
	v_pk_mul_f32 v[124:125], v[28:29], v[124:125] op_sel_hi:[0,1]
	v_mfma_f32_16x16x32_bf16 v[130:133], v[138:141], v[62:65], 0
	v_mul_f32_e64 v122, v28, v122
	v_mul_f32_e64 v123, v28, v123
	v_mfma_f32_16x16x32_bf16 v[134:137], v[138:141], v[46:49], 0
	v_mfma_f32_16x16x32_bf16 v[138:141], v[138:141], v[20:23], 0
	s_waitcnt vmcnt(2)
	v_mfma_f32_16x16x32_bf16 v[126:129], v[144:147], v[0:3], v[126:129]
	v_mfma_f32_16x16x32_bf16 v[130:133], v[144:147], v[58:61], v[130:133]
	v_mfma_f32_16x16x32_bf16 v[134:137], v[144:147], v[42:45], v[134:137]
	v_mfma_f32_16x16x32_bf16 v[138:141], v[144:147], v[16:19], v[138:141]
	s_waitcnt vmcnt(1)
	v_mfma_f32_16x16x32_bf16 v[126:129], v[148:151], v[70:73], v[126:129]
	v_mfma_f32_16x16x32_bf16 v[130:133], v[148:151], v[54:57], v[130:133]
	v_mfma_f32_16x16x32_bf16 v[134:137], v[148:151], v[38:41], v[134:137]
	v_mfma_f32_16x16x32_bf16 v[138:141], v[148:151], v[8:11], v[138:141]
	s_waitcnt vmcnt(0)
	v_mfma_f32_16x16x32_bf16 v[126:129], v[152:155], v[66:69], v[126:129]
	v_mfma_f32_16x16x32_bf16 v[130:133], v[152:155], v[50:53], v[130:133]
	v_mfma_f32_16x16x32_bf16 v[134:137], v[152:155], v[24:27], v[134:137]
	s_nop 5
	v_mul_f32_e64 v128, v180, v128
	v_mul_f32_e64 v129, v180, v129
	v_pk_mul_f32 v[126:127], v[180:181], v[126:127] op_sel_hi:[0,1]
	v_pk_mul_f32 v[132:133], v[176:177], v[132:133] op_sel_hi:[0,1]
	v_mfma_f32_16x16x32_bf16 v[138:141], v[152:155], v[12:15], v[138:141]
	v_add_co_u32_e64 v154, s[0:1], s77, v142
	v_pk_mul_f32 v[130:131], v[176:177], v[130:131] op_sel_hi:[0,1]
	s_nop 0
	v_addc_co_u32_e64 v155, s[0:1], 0, v143, s[0:1]
	global_load_dwordx4 v[142:145], v[154:155], off
	global_load_dwordx4 v[146:149], v[154:155], off offset:64
	global_load_dwordx4 v[150:153], v[154:155], off offset:128
	s_nop 0
	global_load_dwordx4 v[154:157], v[154:155], off offset:192
	s_waitcnt vmcnt(3)
	v_mfma_f32_16x16x32_bf16 v[4:7], v[142:145], v[4:7], 0
	v_mul_f32_e64 v136, v178, v136
	v_mul_f32_e64 v137, v178, v137
	v_pk_mul_f32 v[134:135], v[178:179], v[134:135] op_sel_hi:[0,1]
	s_waitcnt vmcnt(2)
	v_mfma_f32_16x16x32_bf16 v[0:3], v[146:149], v[0:3], v[4:7]
	v_mul_f32_e64 v140, v28, v140
	v_mul_f32_e64 v141, v28, v141
	v_pk_mul_f32 v[138:139], v[28:29], v[138:139] op_sel_hi:[0,1]
	s_add_u32 s0, s30, s18
	s_waitcnt vmcnt(1)
	v_mfma_f32_16x16x32_bf16 v[0:3], v[150:153], v[70:73], v[0:3]
	s_addc_u32 s1, s31, s19
	s_waitcnt vmcnt(0)
	v_mfma_f32_16x16x32_bf16 v[0:3], v[154:157], v[66:69], v[0:3]
	s_nop 7
	v_pk_mul_f32 v[68:69], v[180:181], v[2:3] op_sel_hi:[0,1]
	v_pk_mul_f32 v[66:67], v[180:181], v[0:1] op_sel_hi:[0,1]
	v_mfma_f32_16x16x32_bf16 v[0:3], v[142:145], v[62:65], 0
	v_mfma_f32_16x16x32_bf16 v[0:3], v[146:149], v[58:61], v[0:3]
	v_mfma_f32_16x16x32_bf16 v[0:3], v[150:153], v[54:57], v[0:3]
	v_mfma_f32_16x16x32_bf16 v[0:3], v[154:157], v[50:53], v[0:3]
	s_nop 7
	v_pk_mul_f32 v[72:73], v[176:177], v[2:3] op_sel_hi:[0,1]
	v_pk_mul_f32 v[70:71], v[176:177], v[0:1] op_sel_hi:[0,1]
	v_mfma_f32_16x16x32_bf16 v[0:3], v[142:145], v[46:49], 0
	v_mfma_f32_16x16x32_bf16 v[0:3], v[146:149], v[42:45], v[0:3]
	v_mfma_f32_16x16x32_bf16 v[0:3], v[150:153], v[38:41], v[0:3]
	v_mfma_f32_16x16x32_bf16 v[0:3], v[154:157], v[24:27], v[0:3]
	s_nop 7
	v_pk_mul_f32 v[26:27], v[178:179], v[2:3] op_sel_hi:[0,1]
	v_pk_mul_f32 v[24:25], v[178:179], v[0:1] op_sel_hi:[0,1]
	v_mfma_f32_16x16x32_bf16 v[0:3], v[142:145], v[20:23], 0
	v_mfma_f32_16x16x32_bf16 v[0:3], v[146:149], v[16:19], v[0:3]
	v_mul_f32_e64 v18, v176, v100
	v_mul_f32_e64 v19, v176, v101
	v_pk_mul_f32 v[16:17], v[176:177], v[98:99] op_sel_hi:[0,1]
	v_mfma_f32_16x16x32_bf16 v[0:3], v[150:153], v[8:11], v[0:3]
	v_mfma_f32_16x16x32_bf16 v[0:3], v[154:157], v[12:15], v[0:3]
	s_nop 7
	v_pk_mul_f32 v[10:11], v[28:29], v[2:3] op_sel_hi:[0,1]
	v_pk_mul_f32 v[8:9], v[28:29], v[0:1] op_sel_hi:[0,1]
	ds_read_b64_tr_b16 v[2:3], v214 offset:2560
	ds_read_b64_tr_b16 v[0:1], v214
	ds_read_b64_tr_b16 v[4:5], v214 offset:32
	ds_read_b64_tr_b16 v[12:13], v214 offset:5120
	ds_read_b64_tr_b16 v[14:15], v214 offset:7680
	s_waitcnt lgkmcnt(3)
	v_mfma_f32_16x16x32_bf16 v[94:97], v[0:3], v[30:33], v[94:97]
	v_mfma_f32_16x16x32_bf16 v[50:53], v[0:3], v[74:77], v[16:19]
	v_mfma_f32_16x16x32_bf16 v[16:19], v[0:3], v[78:81], v[102:105]
	v_mfma_f32_16x16x32_bf16 v[0:3], v[0:3], v[82:85], v[106:109]
	s_waitcnt lgkmcnt(0)
	v_mfma_f32_16x16x32_bf16 v[38:41], v[12:15], v[86:89], v[16:19]
	v_mfma_f32_16x16x32_bf16 v[12:15], v[12:15], v[90:93], v[0:3]
	ds_read_b64_tr_b16 v[6:7], v214 offset:2592
	s_nop 3
	ds_read_b64_tr_b16 v[0:1], v214 offset:5152
	ds_read_b64_tr_b16 v[2:3], v214 offset:7712
	s_waitcnt lgkmcnt(2)
	v_mfma_f32_16x16x32_bf16 v[62:65], v[4:7], v[30:33], v[110:113]
	v_mfma_f32_16x16x32_bf16 v[46:49], v[4:7], v[74:77], v[114:117]
	v_mfma_f32_16x16x32_bf16 v[16:19], v[4:7], v[78:81], v[118:121]
	v_mfma_f32_16x16x32_bf16 v[4:7], v[4:7], v[82:85], v[122:125]
	s_waitcnt lgkmcnt(0)
	v_mfma_f32_16x16x32_bf16 v[20:23], v[0:3], v[86:89], v[16:19]
	v_mfma_f32_16x16x32_bf16 v[4:7], v[0:3], v[90:93], v[4:7]
	ds_read_b64_tr_b16 v[0:1], v214 offset:64
	ds_read_b64_tr_b16 v[2:3], v214 offset:2624
	ds_read_b64_tr_b16 v[54:55], v214 offset:5184
	ds_read_b64_tr_b16 v[56:57], v214 offset:7744
	ds_read_b64_tr_b16 v[98:99], v214 offset:96
	ds_read_b64_tr_b16 v[100:101], v214 offset:2656
	ds_read_b64_tr_b16 v[102:103], v214 offset:5216
	ds_read_b64_tr_b16 v[104:105], v214 offset:7776
	s_waitcnt lgkmcnt(6)
	v_mfma_f32_16x16x32_bf16 v[58:61], v[0:3], v[30:33], v[126:129]
	v_mfma_f32_16x16x32_bf16 v[42:45], v[0:3], v[74:77], v[130:133]
	v_mfma_f32_16x16x32_bf16 v[16:19], v[0:3], v[78:81], v[134:137]
	v_mfma_f32_16x16x32_bf16 v[0:3], v[0:3], v[82:85], v[138:141]
	s_waitcnt lgkmcnt(4)
	v_mfma_f32_16x16x32_bf16 v[16:19], v[54:57], v[86:89], v[16:19]
	v_mfma_f32_16x16x32_bf16 v[0:3], v[54:57], v[90:93], v[0:3]
	s_waitcnt lgkmcnt(2)
	v_mfma_f32_16x16x32_bf16 v[54:57], v[98:101], v[30:33], v[66:69]
	v_add_u32_e32 v32, v209, v160
	v_mfma_f32_16x16x32_bf16 v[28:31], v[98:101], v[74:77], v[70:73]
	s_nop 0
	ds_read_b64 v[68:69], v32
	s_nop 0
	global_load_dword v70, v33, s[0:1]
	s_add_u32 s0, s2, s16
	s_addc_u32 s1, s3, s17
	v_mfma_f32_16x16x32_bf16 v[24:27], v[98:101], v[78:81], v[24:27]
	v_mov_b64_e32 v[78:79], s[0:1]
	v_mad_i64_i32 v[66:67], s[0:1], v174, s96, v[78:79]
	v_lshl_add_u64 v[72:73], v[66:67], 0, v[172:173]
	global_load_dwordx2 v[74:75], v[72:73], off
	global_load_dwordx2 v[202:203], v[72:73], off offset:32
	global_load_dwordx2 v[216:217], v[72:73], off offset:64
	global_load_dwordx2 v[248:249], v[72:73], off offset:96
	s_waitcnt lgkmcnt(0)
	v_lshlrev_b32_e32 v66, 16, v68
	v_and_b32_e32 v67, 0xffff0000, v68
	v_lshlrev_b32_e32 v68, 16, v69
	v_and_b32_e32 v69, 0xffff0000, v69
	v_mfma_f32_16x16x32_bf16 v[8:11], v[98:101], v[82:85], v[8:11]
	s_waitcnt vmcnt(4)
	v_pk_fma_f32 v[66:67], v[70:71], v[66:67], v[94:95] op_sel_hi:[0,1,1]
	v_pk_fma_f32 v[68:69], v[70:71], v[68:69], v[96:97] op_sel_hi:[0,1,1]
	v_mfma_f32_16x16x32_bf16 v[24:27], v[102:105], v[86:89], v[24:27]
	s_waitcnt vmcnt(3)
	v_lshlrev_b32_e32 v76, 16, v74
	v_mul_f32_e32 v32, 0xbfb8aa3b, v76
	v_exp_f32_e32 v32, v32
	v_and_b32_e32 v77, 0xffff0000, v74
	v_pk_mul_f32 v[66:67], v[66:67], v[76:77]
	v_lshlrev_b32_e32 v74, 16, v75
	v_add_f32_e32 v32, 1.0, v32
	v_rcp_f32_e32 v80, v32
	v_mul_f32_e32 v32, 0xbfb8aa3b, v77
	v_exp_f32_e32 v32, v32
	v_and_b32_e32 v75, 0xffff0000, v75
	v_pk_mul_f32 v[68:69], v[68:69], v[74:75]
	v_mfma_f32_16x16x32_bf16 v[8:11], v[102:105], v[90:93], v[8:11]
	v_add_f32_e32 v32, 1.0, v32
	v_rcp_f32_e32 v81, v32
	s_nop 0
	v_pk_mul_f32 v[66:67], v[66:67], v[80:81]
	s_nop 0
	v_mul_f32_e32 v32, v67, v67
	v_pk_fma_f32 v[76:77], v[66:67], v[66:67], v[32:33] op_sel_hi:[1,1,0]
	v_mul_f32_e32 v32, 0xbfb8aa3b, v74
	v_exp_f32_e32 v32, v32
	s_nop 0
	v_add_f32_e32 v32, 1.0, v32
	v_rcp_f32_e32 v80, v32
	v_mul_f32_e32 v32, 0xbfb8aa3b, v75
	v_exp_f32_e32 v32, v32
	s_nop 0
	v_add_f32_e32 v32, 1.0, v32
	v_rcp_f32_e32 v81, v32
	s_nop 0
	v_pk_mul_f32 v[68:69], v[68:69], v[80:81]
	v_pk_fma_f32 v[74:75], v[68:69], v[68:69], v[76:77]
	v_mul_f32_e32 v32, v69, v69
	v_pk_add_f32 v[74:75], v[32:33], v[74:75] op_sel_hi:[0,1]
	v_add_u32_e32 v32, v209, v189
	ds_read_b64 v[76:77], v32
	s_waitcnt lgkmcnt(0)
	v_lshlrev_b32_e32 v82, 16, v76
	v_and_b32_e32 v83, 0xffff0000, v76
	v_pk_fma_f32 v[62:63], v[70:71], v[82:83], v[62:63] op_sel_hi:[0,1,1]
	v_lshlrev_b32_e32 v76, 16, v77
	v_and_b32_e32 v77, 0xffff0000, v77
	v_pk_fma_f32 v[64:65], v[70:71], v[76:77], v[64:65] op_sel_hi:[0,1,1]
	s_waitcnt vmcnt(2)
	v_mov_b64_e32 v[80:81], v[202:203]
	v_lshlrev_b32_e32 v84, 16, v80
	v_mul_f32_e32 v32, 0xbfb8aa3b, v84
	v_exp_f32_e32 v32, v32
	v_and_b32_e32 v85, 0xffff0000, v80
	v_pk_mul_f32 v[62:63], v[62:63], v[84:85]
	v_lshlrev_b32_e32 v80, 16, v81
	v_add_f32_e32 v32, 1.0, v32
	v_rcp_f32_e32 v86, v32
	v_mul_f32_e32 v32, 0xbfb8aa3b, v85
	v_exp_f32_e32 v32, v32
	v_and_b32_e32 v81, 0xffff0000, v81
	v_pk_mul_f32 v[64:65], v[64:65], v[80:81]
	v_add_f32_e32 v32, 1.0, v32
	v_rcp_f32_e32 v87, v32
	s_nop 0
	v_pk_mul_f32 v[62:63], v[62:63], v[86:87]
	s_nop 0
	v_pk_fma_f32 v[74:75], v[62:63], v[62:63], v[74:75]
	v_mul_f32_e32 v32, v63, v63
	v_pk_add_f32 v[74:75], v[32:33], v[74:75] op_sel_hi:[0,1]
	v_mul_f32_e32 v32, 0xbfb8aa3b, v80
	v_exp_f32_e32 v32, v32
	s_nop 0
	v_add_f32_e32 v32, 1.0, v32
	v_rcp_f32_e32 v82, v32
	v_mul_f32_e32 v32, 0xbfb8aa3b, v81
	v_exp_f32_e32 v32, v32
	s_waitcnt vmcnt(1)
	v_mov_b64_e32 v[80:81], v[216:217]
	v_lshlrev_b32_e32 v84, 16, v80
	v_add_f32_e32 v32, 1.0, v32
	v_rcp_f32_e32 v83, v32
	v_and_b32_e32 v85, 0xffff0000, v80
	v_lshlrev_b32_e32 v80, 16, v81
	v_and_b32_e32 v81, 0xffff0000, v81
	v_pk_mul_f32 v[64:65], v[64:65], v[82:83]
	s_nop 0
	v_pk_fma_f32 v[74:75], v[64:65], v[64:65], v[74:75]
	v_mul_f32_e32 v32, v65, v65
	v_pk_add_f32 v[74:75], v[32:33], v[74:75] op_sel_hi:[0,1]
	v_add_u32_e32 v32, v209, v188
	ds_read_b64 v[76:77], v32
	v_mul_f32_e32 v32, 0xbfb8aa3b, v84
	v_exp_f32_e32 v32, v32
	s_waitcnt lgkmcnt(0)
	v_lshlrev_b32_e32 v82, 16, v76
	v_add_f32_e32 v32, 1.0, v32
	v_rcp_f32_e32 v86, v32
	v_mul_f32_e32 v32, 0xbfb8aa3b, v85
	v_exp_f32_e32 v32, v32
	v_and_b32_e32 v83, 0xffff0000, v76
	v_pk_fma_f32 v[58:59], v[70:71], v[82:83], v[58:59] op_sel_hi:[0,1,1]
	v_pk_mul_f32 v[58:59], v[58:59], v[84:85]
	v_add_f32_e32 v32, 1.0, v32
	v_rcp_f32_e32 v87, v32
	v_lshlrev_b32_e32 v76, 16, v77
	v_and_b32_e32 v77, 0xffff0000, v77
	v_pk_fma_f32 v[60:61], v[70:71], v[76:77], v[60:61] op_sel_hi:[0,1,1]
	v_pk_mul_f32 v[58:59], v[58:59], v[86:87]
	v_pk_mul_f32 v[60:61], v[60:61], v[80:81]
	v_pk_fma_f32 v[74:75], v[58:59], v[58:59], v[74:75]
	v_mul_f32_e32 v32, v59, v59
	v_pk_add_f32 v[74:75], v[32:33], v[74:75] op_sel_hi:[0,1]
	v_mul_f32_e32 v32, 0xbfb8aa3b, v80
	v_exp_f32_e32 v32, v32
	s_nop 0
	v_add_f32_e32 v32, 1.0, v32
	v_rcp_f32_e32 v82, v32
	v_mul_f32_e32 v32, 0xbfb8aa3b, v81
	v_exp_f32_e32 v32, v32
	s_nop 0
	v_add_f32_e32 v32, 1.0, v32
	v_rcp_f32_e32 v83, v32
	s_nop 0
	v_pk_mul_f32 v[60:61], v[60:61], v[82:83]
	s_nop 0
	v_pk_fma_f32 v[74:75], v[60:61], v[60:61], v[74:75]
	v_mul_f32_e32 v32, v61, v61
	v_pk_add_f32 v[74:75], v[32:33], v[74:75] op_sel_hi:[0,1]
	v_add_u32_e32 v32, v209, v187
	ds_read_b64 v[76:77], v32
	s_waitcnt lgkmcnt(0)
	v_lshlrev_b32_e32 v72, 16, v76
	v_and_b32_e32 v73, 0xffff0000, v76
	v_pk_fma_f32 v[54:55], v[70:71], v[72:73], v[54:55] op_sel_hi:[0,1,1]
	s_waitcnt vmcnt(0)
	v_mov_b64_e32 v[80:81], v[248:249]
	v_lshlrev_b32_e32 v82, 16, v80
	v_mul_f32_e32 v32, 0xbfb8aa3b, v82
	v_exp_f32_e32 v32, v32
	v_and_b32_e32 v83, 0xffff0000, v80
	v_pk_mul_f32 v[54:55], v[54:55], v[82:83]
	v_lshlrev_b32_e32 v76, 16, v81
	v_add_f32_e32 v32, 1.0, v32
	v_rcp_f32_e32 v84, v32
	v_mul_f32_e32 v32, 0xbfb8aa3b, v83
	v_exp_f32_e32 v32, v32
	s_nop 0
	v_add_f32_e32 v32, 1.0, v32
	v_rcp_f32_e32 v85, v32
	s_nop 0
	v_pk_mul_f32 v[72:73], v[54:55], v[84:85]
	s_nop 0
	v_pk_fma_f32 v[54:55], v[72:73], v[72:73], v[74:75]
	v_mul_f32_e32 v32, v73, v73
	v_pk_add_f32 v[54:55], v[32:33], v[54:55] op_sel_hi:[0,1]
	v_mul_f32_e32 v32, 0xbfb8aa3b, v76
	v_exp_f32_e32 v32, v32
	v_lshlrev_b32_e32 v74, 16, v77
	v_and_b32_e32 v75, 0xffff0000, v77
	v_and_b32_e32 v77, 0xffff0000, v81
	v_add_f32_e32 v32, 1.0, v32
	v_rcp_f32_e32 v80, v32
	v_mul_f32_e32 v32, 0xbfb8aa3b, v77
	v_exp_f32_e32 v32, v32
	v_pk_fma_f32 v[56:57], v[70:71], v[74:75], v[56:57] op_sel_hi:[0,1,1]
	v_pk_mul_f32 v[56:57], v[56:57], v[76:77]
	v_or_b32_e32 v76, s55, v185
	v_add_f32_e32 v32, 1.0, v32
	v_rcp_f32_e32 v81, v32
	s_nop 0
	v_pk_mul_f32 v[56:57], v[56:57], v[80:81]
	s_nop 0
	v_pk_fma_f32 v[54:55], v[56:57], v[56:57], v[54:55]
	v_mul_f32_e32 v32, v57, v57
	v_pk_add_f32 v[110:111], v[32:33], v[54:55] op_sel_hi:[0,1]
	v_or_b32_e32 v54, s55, v184
	v_mad_i64_i32 v[74:75], s[0:1], v54, s96, v[78:79]
	v_lshl_add_u64 v[74:75], v[74:75], 0, v[172:173]
	global_load_dwordx2 v[126:127], v[74:75], off
	global_load_dwordx2 v[122:123], v[74:75], off offset:32
	global_load_dwordx2 v[116:117], v[74:75], off offset:64
	global_load_dwordx2 v[112:113], v[74:75], off offset:96
	v_mad_i64_i32 v[74:75], s[0:1], v76, s96, v[78:79]
	v_lshl_add_u64 v[74:75], v[74:75], 0, v[172:173]
	global_load_dwordx2 v[106:107], v[74:75], off
	global_load_dwordx2 v[102:103], v[74:75], off offset:32
	global_load_dwordx2 v[98:99], v[74:75], off offset:64
	global_load_dwordx2 v[94:95], v[74:75], off offset:96
	v_or_b32_e32 v74, s55, v186
	v_mad_i64_i32 v[78:79], s[0:1], v74, s96, v[78:79]
	v_lshl_add_u64 v[78:79], v[78:79], 0, v[172:173]
	global_load_dwordx2 v[90:91], v[78:79], off
	global_load_dwordx2 v[86:87], v[78:79], off offset:32
	global_load_dwordx2 v[82:83], v[78:79], off offset:64
	v_add_u32_e32 v32, v211, v160
	global_load_dwordx2 v[78:79], v[78:79], off offset:96
	ds_read_b64 v[120:121], v32
	v_add_u32_e32 v32, v211, v189
	ds_read_b64 v[124:125], v32
	v_add_u32_e32 v32, v211, v188
	ds_read_b64 v[118:119], v32
	v_add_u32_e32 v32, v211, v187
	ds_read_b64 v[114:115], v32
	v_add_u32_e32 v32, v212, v160
	ds_read_b64 v[108:109], v32
	v_add_u32_e32 v32, v212, v189
	ds_read_b64 v[104:105], v32
	v_add_u32_e32 v32, v212, v188
	ds_read_b64 v[100:101], v32
	v_add_u32_e32 v32, v212, v187
	ds_read_b64 v[96:97], v32
	v_add_u32_e32 v32, v210, v160
	ds_read_b64 v[92:93], v32
	v_add_u32_e32 v32, v210, v189
	ds_read_b64 v[88:89], v32
	v_add_u32_e32 v32, v210, v188
	ds_read_b64 v[84:85], v32
	v_add_u32_e32 v32, v210, v187
	ds_read_b64 v[80:81], v32
	s_lshl_b32 s0, s33, 11
	v_mov_b32_e32 v55, v110
	s_add_i32 s16, s0, 0
	s_nop 0
	v_permlane16_swap_b32_e32 v110, v55
	s_add_i32 s16, s16, 0x15000
	v_add_f32_e32 v55, v110, v55
	s_add_i32 s0, s16, s35
	v_mov_b32_e32 v71, v55
	v_lshl_add_u32 v32, v166, 2, s0
	s_nop 0
	v_permlane32_swap_b32_e32 v55, v71
	s_and_saveexec_b64 s[0:1], s[42:43]
	v_add_f32_e32 v55, v55, v71
	ds_write_b32 v32, v55
	s_or_b64 exec, exec, s[0:1]
	s_waitcnt vmcnt(11)
	v_lshlrev_b32_e32 v128, 16, v126
	v_mul_f32_e32 v55, 0xbfb8aa3b, v128
	v_exp_f32_e32 v55, v55
	v_and_b32_e32 v129, 0xffff0000, v126
	v_lshlrev_b32_e32 v126, 16, v127
	v_mov_b32_e32 v71, v70
	v_add_f32_e32 v55, 1.0, v55
	v_rcp_f32_e32 v130, v55
	v_mul_f32_e32 v55, 0xbfb8aa3b, v129
	v_exp_f32_e32 v55, v55
	s_waitcnt lgkmcnt(11)
	v_lshlrev_b32_e32 v110, 16, v120
	v_and_b32_e32 v111, 0xffff0000, v120
	v_pk_fma_f32 v[50:51], v[70:71], v[110:111], v[50:51]
	v_add_f32_e32 v55, 1.0, v55
	v_rcp_f32_e32 v131, v55
	v_mul_f32_e32 v55, 0xbfb8aa3b, v126
	v_exp_f32_e32 v55, v55
	v_and_b32_e32 v127, 0xffff0000, v127
	v_pk_mul_f32 v[50:51], v[50:51], v[128:129]
	v_lshlrev_b32_e32 v120, 16, v121
	v_add_f32_e32 v55, 1.0, v55
	v_rcp_f32_e32 v128, v55
	v_mul_f32_e32 v55, 0xbfb8aa3b, v127
	v_exp_f32_e32 v55, v55
	v_and_b32_e32 v121, 0xffff0000, v121
	v_pk_fma_f32 v[52:53], v[70:71], v[120:121], v[52:53]
	v_pk_mul_f32 v[50:51], v[50:51], v[130:131]
	v_pk_mul_f32 v[52:53], v[52:53], v[126:127]
	v_add_f32_e32 v55, 1.0, v55
	s_waitcnt vmcnt(10)
	v_lshlrev_b32_e32 v126, 16, v122
	v_rcp_f32_e32 v129, v55
	v_mul_f32_e32 v55, 0xbfb8aa3b, v126
	v_exp_f32_e32 v55, v55
	v_and_b32_e32 v127, 0xffff0000, v122
	v_pk_mul_f32 v[52:53], v[52:53], v[128:129]
	v_lshlrev_b32_e32 v122, 16, v123
	v_add_f32_e32 v55, 1.0, v55
	v_rcp_f32_e32 v128, v55
	v_mul_f32_e32 v55, 0xbfb8aa3b, v127
	v_exp_f32_e32 v55, v55
	v_mul_f32_e32 v110, v51, v51
	v_pk_fma_f32 v[110:111], v[50:51], v[50:51], v[110:111] op_sel_hi:[1,1,0]
	v_mul_f32_e32 v120, v53, v53
	v_add_f32_e32 v55, 1.0, v55
	v_rcp_f32_e32 v129, v55
	v_mul_f32_e32 v55, 0xbfb8aa3b, v122
	v_exp_f32_e32 v55, v55
	v_pk_fma_f32 v[110:111], v[52:53], v[52:53], v[110:111]
	v_and_b32_e32 v123, 0xffff0000, v123
	v_pk_add_f32 v[110:111], v[120:121], v[110:111] op_sel_hi:[0,1]
	s_waitcnt lgkmcnt(10)
	v_lshlrev_b32_e32 v120, 16, v124
	v_and_b32_e32 v121, 0xffff0000, v124
	v_pk_fma_f32 v[46:47], v[70:71], v[120:121], v[46:47]
	v_add_f32_e32 v55, 1.0, v55
	v_pk_mul_f32 v[46:47], v[46:47], v[126:127]
	v_rcp_f32_e32 v124, v55
	v_mul_f32_e32 v55, 0xbfb8aa3b, v123
	v_pk_mul_f32 v[46:47], v[46:47], v[128:129]
	v_exp_f32_e32 v55, v55
	v_pk_fma_f32 v[110:111], v[46:47], v[46:47], v[110:111]
	v_mul_f32_e32 v120, v47, v47
	v_pk_add_f32 v[110:111], v[120:121], v[110:111] op_sel_hi:[0,1]
	v_lshlrev_b32_e32 v120, 16, v125
	v_and_b32_e32 v121, 0xffff0000, v125
	v_pk_fma_f32 v[48:49], v[70:71], v[120:121], v[48:49]
	v_add_f32_e32 v55, 1.0, v55
	v_pk_mul_f32 v[48:49], v[48:49], v[122:123]
	s_waitcnt vmcnt(9)
	v_lshlrev_b32_e32 v122, 16, v116
	v_rcp_f32_e32 v125, v55
	v_mul_f32_e32 v55, 0xbfb8aa3b, v122
	v_exp_f32_e32 v55, v55
	v_and_b32_e32 v123, 0xffff0000, v116
	v_pk_mul_f32 v[48:49], v[48:49], v[124:125]
	v_add_f32_e32 v55, 1.0, v55
	v_rcp_f32_e32 v124, v55
	v_mul_f32_e32 v55, 0xbfb8aa3b, v123
	v_exp_f32_e32 v55, v55
	v_pk_fma_f32 v[110:111], v[48:49], v[48:49], v[110:111]
	v_mul_f32_e32 v120, v49, v49
	v_pk_add_f32 v[110:111], v[120:121], v[110:111] op_sel_hi:[0,1]
	v_add_f32_e32 v55, 1.0, v55
	v_rcp_f32_e32 v125, v55
	s_waitcnt lgkmcnt(9)
	v_lshlrev_b32_e32 v120, 16, v118
	v_and_b32_e32 v121, 0xffff0000, v118
	v_pk_fma_f32 v[42:43], v[70:71], v[120:121], v[42:43]
	v_lshlrev_b32_e32 v118, 16, v119
	v_pk_mul_f32 v[42:43], v[42:43], v[122:123]
	v_and_b32_e32 v119, 0xffff0000, v119
	v_pk_mul_f32 v[42:43], v[42:43], v[124:125]
	v_pk_fma_f32 v[44:45], v[70:71], v[118:119], v[44:45]
	v_pk_fma_f32 v[110:111], v[42:43], v[42:43], v[110:111]
	v_mul_f32_e32 v116, v43, v43
	v_pk_add_f32 v[110:111], v[116:117], v[110:111] op_sel_hi:[0,1]
	v_lshlrev_b32_e32 v116, 16, v117
	v_mul_f32_e32 v55, 0xbfb8aa3b, v116
	v_exp_f32_e32 v55, v55
	v_and_b32_e32 v117, 0xffff0000, v117
	s_waitcnt vmcnt(8)
	v_lshlrev_b32_e32 v118, 16, v112
	v_pk_mul_f32 v[44:45], v[44:45], v[116:117]
	v_add_f32_e32 v55, 1.0, v55
	v_rcp_f32_e32 v120, v55
	v_mul_f32_e32 v55, 0xbfb8aa3b, v117
	v_exp_f32_e32 v55, v55
	v_and_b32_e32 v119, 0xffff0000, v112
	v_add_f32_e32 v55, 1.0, v55
	v_rcp_f32_e32 v121, v55
	v_mul_f32_e32 v55, 0xbfb8aa3b, v118
	v_exp_f32_e32 v55, v55
	v_pk_mul_f32 v[44:45], v[44:45], v[120:121]
	s_nop 0
	v_pk_fma_f32 v[110:111], v[44:45], v[44:45], v[110:111]
	v_add_f32_e32 v55, 1.0, v55
	v_rcp_f32_e32 v120, v55
	v_mul_f32_e32 v55, 0xbfb8aa3b, v119
	v_exp_f32_e32 v55, v55
	v_mul_f32_e32 v116, v45, v45
	v_pk_add_f32 v[110:111], v[116:117], v[110:111] op_sel_hi:[0,1]
	s_waitcnt lgkmcnt(8)
	v_lshlrev_b32_e32 v116, 16, v114
	v_add_f32_e32 v55, 1.0, v55
	v_rcp_f32_e32 v121, v55
	v_and_b32_e32 v117, 0xffff0000, v114
	v_pk_fma_f32 v[28:29], v[70:71], v[116:117], v[28:29]
	v_lshlrev_b32_e32 v114, 16, v115
	v_pk_mul_f32 v[28:29], v[28:29], v[118:119]
	v_and_b32_e32 v115, 0xffff0000, v115
	v_pk_mul_f32 v[28:29], v[28:29], v[120:121]
	v_pk_fma_f32 v[30:31], v[70:71], v[114:115], v[30:31]
	v_pk_fma_f32 v[110:111], v[28:29], v[28:29], v[110:111]
	v_mul_f32_e32 v112, v29, v29
	v_pk_add_f32 v[110:111], v[112:113], v[110:111] op_sel_hi:[0,1]
	v_lshlrev_b32_e32 v112, 16, v113
	v_mul_f32_e32 v55, 0xbfb8aa3b, v112
	v_exp_f32_e32 v55, v55
	v_and_b32_e32 v113, 0xffff0000, v113
	v_pk_mul_f32 v[30:31], v[30:31], v[112:113]
	v_add_f32_e32 v55, 1.0, v55
	v_rcp_f32_e32 v116, v55
	v_mul_f32_e32 v55, 0xbfb8aa3b, v113
	v_exp_f32_e32 v55, v55
	s_nop 0
	v_add_f32_e32 v55, 1.0, v55
	v_rcp_f32_e32 v117, v55
	s_nop 0
	v_pk_mul_f32 v[30:31], v[30:31], v[116:117]
	s_nop 0
	v_pk_fma_f32 v[110:111], v[30:31], v[30:31], v[110:111]
	v_mul_f32_e32 v112, v31, v31
	v_pk_add_f32 v[110:111], v[112:113], v[110:111] op_sel_hi:[0,1]
	v_mov_b32_e32 v55, v110
	s_nop 1
	v_permlane16_swap_b32_e32 v110, v55
	v_add_f32_e32 v55, v110, v55
	v_mov_b32_e32 v75, v55
	s_nop 1
	v_permlane32_swap_b32_e32 v55, v75
	s_and_saveexec_b64 s[0:1], s[42:43]
	v_add_f32_e32 v55, v55, v75
	ds_write_b32 v32, v55 offset:64
	s_or_b64 exec, exec, s[0:1]
	s_waitcnt vmcnt(7)
	v_lshlrev_b32_e32 v112, 16, v106
	v_mul_f32_e32 v55, 0xbfb8aa3b, v112
	v_exp_f32_e32 v55, v55
	v_and_b32_e32 v113, 0xffff0000, v106
	s_waitcnt lgkmcnt(7)
	v_lshlrev_b32_e32 v110, 16, v108
	v_and_b32_e32 v111, 0xffff0000, v108
	v_add_f32_e32 v55, 1.0, v55
	v_rcp_f32_e32 v114, v55
	v_mul_f32_e32 v55, 0xbfb8aa3b, v113
	v_exp_f32_e32 v55, v55
	v_pk_fma_f32 v[38:39], v[70:71], v[110:111], v[38:39]
	v_lshlrev_b32_e32 v108, 16, v109
	v_pk_mul_f32 v[38:39], v[38:39], v[112:113]
	v_add_f32_e32 v55, 1.0, v55
	v_rcp_f32_e32 v115, v55
	v_and_b32_e32 v109, 0xffff0000, v109
	v_pk_fma_f32 v[40:41], v[70:71], v[108:109], v[40:41]
	v_pk_mul_f32 v[38:39], v[38:39], v[114:115]
	s_nop 0
	v_mul_f32_e32 v106, v39, v39
	v_pk_fma_f32 v[110:111], v[38:39], v[38:39], v[106:107] op_sel_hi:[1,1,0]
	v_lshlrev_b32_e32 v106, 16, v107
	v_mul_f32_e32 v55, 0xbfb8aa3b, v106
	v_exp_f32_e32 v55, v55
	v_and_b32_e32 v107, 0xffff0000, v107
	v_pk_mul_f32 v[40:41], v[40:41], v[106:107]
	v_add_f32_e32 v55, 1.0, v55
	v_rcp_f32_e32 v112, v55
	v_mul_f32_e32 v55, 0xbfb8aa3b, v107
	v_exp_f32_e32 v55, v55
	s_nop 0
	v_add_f32_e32 v55, 1.0, v55
	v_rcp_f32_e32 v113, v55
	s_nop 0
	v_pk_mul_f32 v[40:41], v[40:41], v[112:113]
	s_nop 0
	v_pk_fma_f32 v[106:107], v[40:41], v[40:41], v[110:111]
	s_waitcnt vmcnt(6)
	v_lshlrev_b32_e32 v110, 16, v102
	v_mul_f32_e32 v55, 0xbfb8aa3b, v110
	v_exp_f32_e32 v55, v55
	v_and_b32_e32 v111, 0xffff0000, v102
	v_mul_f32_e32 v108, v41, v41
	v_pk_add_f32 v[106:107], v[108:109], v[106:107] op_sel_hi:[0,1]
	v_add_f32_e32 v55, 1.0, v55
	v_rcp_f32_e32 v112, v55
	v_mul_f32_e32 v55, 0xbfb8aa3b, v111
	v_exp_f32_e32 v55, v55
	s_waitcnt lgkmcnt(6)
	v_lshlrev_b32_e32 v108, 16, v104
	v_and_b32_e32 v109, 0xffff0000, v104
	v_pk_fma_f32 v[20:21], v[70:71], v[108:109], v[20:21]
	v_add_f32_e32 v55, 1.0, v55
	v_rcp_f32_e32 v113, v55
	v_pk_mul_f32 v[20:21], v[20:21], v[110:111]
	v_lshlrev_b32_e32 v104, 16, v105
	v_and_b32_e32 v105, 0xffff0000, v105
	v_pk_mul_f32 v[20:21], v[20:21], v[112:113]
	v_pk_fma_f32 v[22:23], v[70:71], v[104:105], v[22:23]
	v_pk_fma_f32 v[106:107], v[20:21], v[20:21], v[106:107]
	v_mul_f32_e32 v102, v21, v21
	v_pk_add_f32 v[106:107], v[102:103], v[106:107] op_sel_hi:[0,1]
	v_lshlrev_b32_e32 v102, 16, v103
	v_mul_f32_e32 v55, 0xbfb8aa3b, v102
	v_exp_f32_e32 v55, v55
	v_and_b32_e32 v103, 0xffff0000, v103
	v_pk_mul_f32 v[22:23], v[22:23], v[102:103]
	v_add_f32_e32 v55, 1.0, v55
	v_rcp_f32_e32 v108, v55
	v_mul_f32_e32 v55, 0xbfb8aa3b, v103
	v_exp_f32_e32 v55, v55
	s_nop 0
	v_add_f32_e32 v55, 1.0, v55
	v_rcp_f32_e32 v109, v55
	s_nop 0
	v_pk_mul_f32 v[22:23], v[22:23], v[108:109]
	s_nop 0
	v_pk_fma_f32 v[102:103], v[22:23], v[22:23], v[106:107]
	s_waitcnt vmcnt(5)
	v_lshlrev_b32_e32 v106, 16, v98
	v_mul_f32_e32 v55, 0xbfb8aa3b, v106
	v_exp_f32_e32 v55, v55
	v_and_b32_e32 v107, 0xffff0000, v98
	v_mul_f32_e32 v104, v23, v23
	v_pk_add_f32 v[102:103], v[104:105], v[102:103] op_sel_hi:[0,1]
	v_add_f32_e32 v55, 1.0, v55
	v_rcp_f32_e32 v108, v55
	v_mul_f32_e32 v55, 0xbfb8aa3b, v107
	v_exp_f32_e32 v55, v55
	s_waitcnt lgkmcnt(5)
	v_lshlrev_b32_e32 v104, 16, v100
	v_and_b32_e32 v105, 0xffff0000, v100
	v_pk_fma_f32 v[16:17], v[70:71], v[104:105], v[16:17]
	v_add_f32_e32 v55, 1.0, v55
	v_rcp_f32_e32 v109, v55
	v_pk_mul_f32 v[16:17], v[16:17], v[106:107]
	v_lshlrev_b32_e32 v100, 16, v101
	v_and_b32_e32 v101, 0xffff0000, v101
	v_pk_mul_f32 v[16:17], v[16:17], v[108:109]
	v_pk_fma_f32 v[18:19], v[70:71], v[100:101], v[18:19]
	v_pk_fma_f32 v[102:103], v[16:17], v[16:17], v[102:103]
	v_mul_f32_e32 v98, v17, v17
	v_pk_add_f32 v[102:103], v[98:99], v[102:103] op_sel_hi:[0,1]
	v_lshlrev_b32_e32 v98, 16, v99
	v_mul_f32_e32 v55, 0xbfb8aa3b, v98
	v_exp_f32_e32 v55, v55
	v_and_b32_e32 v99, 0xffff0000, v99
	v_pk_mul_f32 v[18:19], v[18:19], v[98:99]
	v_add_f32_e32 v55, 1.0, v55
	v_rcp_f32_e32 v104, v55
	v_mul_f32_e32 v55, 0xbfb8aa3b, v99
	v_exp_f32_e32 v55, v55
	s_nop 0
	v_add_f32_e32 v55, 1.0, v55
	v_rcp_f32_e32 v105, v55
	s_nop 0
	v_pk_mul_f32 v[18:19], v[18:19], v[104:105]
	s_nop 0
	v_pk_fma_f32 v[98:99], v[18:19], v[18:19], v[102:103]
	s_waitcnt vmcnt(4)
	v_lshlrev_b32_e32 v102, 16, v94
	v_mul_f32_e32 v55, 0xbfb8aa3b, v102
	v_exp_f32_e32 v55, v55
	v_and_b32_e32 v103, 0xffff0000, v94
	v_mul_f32_e32 v100, v19, v19
	v_pk_add_f32 v[98:99], v[100:101], v[98:99] op_sel_hi:[0,1]
	v_add_f32_e32 v55, 1.0, v55
	v_rcp_f32_e32 v104, v55
	v_mul_f32_e32 v55, 0xbfb8aa3b, v103
	v_exp_f32_e32 v55, v55
	s_waitcnt lgkmcnt(4)
	v_lshlrev_b32_e32 v100, 16, v96
	v_and_b32_e32 v101, 0xffff0000, v96
	v_pk_fma_f32 v[24:25], v[70:71], v[100:101], v[24:25]
	v_add_f32_e32 v55, 1.0, v55
	v_rcp_f32_e32 v105, v55
	v_pk_mul_f32 v[24:25], v[24:25], v[102:103]
	v_lshlrev_b32_e32 v96, 16, v97
	v_and_b32_e32 v97, 0xffff0000, v97
	v_pk_mul_f32 v[24:25], v[24:25], v[104:105]
	v_pk_fma_f32 v[26:27], v[70:71], v[96:97], v[26:27]
	v_pk_fma_f32 v[98:99], v[24:25], v[24:25], v[98:99]
	v_mul_f32_e32 v94, v25, v25
	v_pk_add_f32 v[98:99], v[94:95], v[98:99] op_sel_hi:[0,1]
	v_lshlrev_b32_e32 v94, 16, v95
	v_mul_f32_e32 v55, 0xbfb8aa3b, v94
	v_exp_f32_e32 v55, v55
	v_and_b32_e32 v95, 0xffff0000, v95
	v_pk_mul_f32 v[26:27], v[26:27], v[94:95]
	v_add_f32_e32 v55, 1.0, v55
	v_rcp_f32_e32 v100, v55
	v_mul_f32_e32 v55, 0xbfb8aa3b, v95
	v_exp_f32_e32 v55, v55
	s_nop 0
	v_add_f32_e32 v55, 1.0, v55
	v_rcp_f32_e32 v101, v55
	s_nop 0
	v_pk_mul_f32 v[26:27], v[26:27], v[100:101]
	s_nop 0
	v_pk_fma_f32 v[94:95], v[26:27], v[26:27], v[98:99]
	v_mul_f32_e32 v96, v27, v27
	v_pk_add_f32 v[94:95], v[96:97], v[94:95] op_sel_hi:[0,1]
	v_mov_b32_e32 v55, v94
	s_nop 1
	v_permlane16_swap_b32_e32 v94, v55
	v_add_f32_e32 v55, v94, v55
	v_mov_b32_e32 v75, v55
	s_nop 1
	v_permlane32_swap_b32_e32 v55, v75
	s_and_saveexec_b64 s[0:1], s[42:43]
	v_add_f32_e32 v55, v55, v75
	ds_write_b32 v32, v55 offset:128
	s_or_b64 exec, exec, s[0:1]
	s_waitcnt vmcnt(3)
	v_lshlrev_b32_e32 v96, 16, v90
	v_mul_f32_e32 v55, 0xbfb8aa3b, v96
	v_exp_f32_e32 v55, v55
	v_and_b32_e32 v97, 0xffff0000, v90
	v_lshlrev_b32_e32 v90, 16, v91
	s_waitcnt lgkmcnt(3)
	v_lshlrev_b32_e32 v94, 16, v92
	v_add_f32_e32 v55, 1.0, v55
	v_rcp_f32_e32 v98, v55
	v_mul_f32_e32 v55, 0xbfb8aa3b, v97
	v_exp_f32_e32 v55, v55
	v_and_b32_e32 v95, 0xffff0000, v92
	v_pk_fma_f32 v[12:13], v[70:71], v[94:95], v[12:13]
	v_and_b32_e32 v91, 0xffff0000, v91
	v_add_f32_e32 v55, 1.0, v55
	v_rcp_f32_e32 v99, v55
	v_mul_f32_e32 v55, 0xbfb8aa3b, v90
	v_exp_f32_e32 v55, v55
	v_pk_mul_f32 v[12:13], v[12:13], v[96:97]
	v_lshlrev_b32_e32 v92, 16, v93
	v_and_b32_e32 v93, 0xffff0000, v93
	v_add_f32_e32 v55, 1.0, v55
	v_rcp_f32_e32 v96, v55
	v_mul_f32_e32 v55, 0xbfb8aa3b, v91
	v_exp_f32_e32 v55, v55
	v_pk_mul_f32 v[94:95], v[12:13], v[98:99]
	v_pk_fma_f32 v[14:15], v[70:71], v[92:93], v[14:15]
	v_mul_f32_e32 v12, v95, v95
	v_add_f32_e32 v55, 1.0, v55
	v_rcp_f32_e32 v97, v55
	v_pk_mul_f32 v[14:15], v[14:15], v[90:91]
	v_pk_fma_f32 v[12:13], v[94:95], v[94:95], v[12:13] op_sel_hi:[1,1,0]
	s_waitcnt vmcnt(2)
	v_lshlrev_b32_e32 v92, 16, v86
	v_pk_mul_f32 v[90:91], v[14:15], v[96:97]
	v_and_b32_e32 v93, 0xffff0000, v86
	v_pk_fma_f32 v[12:13], v[90:91], v[90:91], v[12:13]
	v_mul_f32_e32 v14, v91, v91
	v_pk_add_f32 v[12:13], v[14:15], v[12:13] op_sel_hi:[0,1]
	s_waitcnt lgkmcnt(2)
	v_lshlrev_b32_e32 v14, 16, v88
	v_and_b32_e32 v15, 0xffff0000, v88
	v_mul_f32_e32 v55, 0xbfb8aa3b, v92
	v_pk_fma_f32 v[4:5], v[70:71], v[14:15], v[4:5]
	v_mul_f32_e32 v14, 0xbfb8aa3b, v93
	v_exp_f32_e32 v55, v55
	v_exp_f32_e32 v14, v14
	v_pk_mul_f32 v[4:5], v[4:5], v[92:93]
	v_and_b32_e32 v15, 0xffff0000, v87
	v_add_f32_e32 v55, 1.0, v55
	v_add_f32_e32 v14, 1.0, v14
	v_rcp_f32_e32 v96, v55
	v_rcp_f32_e32 v97, v14
	v_lshlrev_b32_e32 v14, 16, v87
	v_mul_f32_e32 v55, 0xbfb8aa3b, v14
	v_exp_f32_e32 v55, v55
	v_pk_mul_f32 v[92:93], v[4:5], v[96:97]
	v_add_f32_e32 v55, 1.0, v55
	v_pk_fma_f32 v[4:5], v[92:93], v[92:93], v[12:13]
	v_mul_f32_e32 v12, v93, v93
	v_pk_add_f32 v[4:5], v[12:13], v[4:5] op_sel_hi:[0,1]
	v_lshlrev_b32_e32 v12, 16, v89
	v_and_b32_e32 v13, 0xffff0000, v89
	v_pk_fma_f32 v[6:7], v[70:71], v[12:13], v[6:7]
	v_mul_f32_e32 v12, 0xbfb8aa3b, v15
	v_exp_f32_e32 v12, v12
	v_rcp_f32_e32 v86, v55
	v_pk_mul_f32 v[6:7], v[6:7], v[14:15]
	s_waitcnt vmcnt(1)
	v_and_b32_e32 v13, 0xffff0000, v82
	v_add_f32_e32 v12, 1.0, v12
	v_rcp_f32_e32 v87, v12
	v_lshlrev_b32_e32 v12, 16, v82
	v_mul_f32_e32 v14, 0xbfb8aa3b, v12
	v_exp_f32_e32 v14, v14
	v_pk_mul_f32 v[86:87], v[6:7], v[86:87]
	v_add_f32_e32 v14, 1.0, v14
	v_pk_fma_f32 v[4:5], v[86:87], v[86:87], v[4:5]
	v_mul_f32_e32 v6, v87, v87
	v_pk_add_f32 v[4:5], v[6:7], v[4:5] op_sel_hi:[0,1]
	s_waitcnt lgkmcnt(1)
	v_lshlrev_b32_e32 v6, 16, v84
	v_and_b32_e32 v7, 0xffff0000, v84
	v_pk_fma_f32 v[0:1], v[70:71], v[6:7], v[0:1]
	v_mul_f32_e32 v6, 0xbfb8aa3b, v13
	v_exp_f32_e32 v6, v6
	v_rcp_f32_e32 v14, v14
	v_pk_mul_f32 v[0:1], v[0:1], v[12:13]
	v_and_b32_e32 v7, 0xffff0000, v83
	v_add_f32_e32 v6, 1.0, v6
	v_rcp_f32_e32 v15, v6
	v_lshlrev_b32_e32 v6, 16, v83
	v_mul_f32_e32 v12, 0xbfb8aa3b, v6
	v_exp_f32_e32 v12, v12
	v_pk_mul_f32 v[88:89], v[0:1], v[14:15]
	v_add_f32_e32 v12, 1.0, v12
	v_pk_fma_f32 v[0:1], v[88:89], v[88:89], v[4:5]
	v_mul_f32_e32 v4, v89, v89
	v_pk_add_f32 v[0:1], v[4:5], v[0:1] op_sel_hi:[0,1]
	v_lshlrev_b32_e32 v4, 16, v85
	v_and_b32_e32 v5, 0xffff0000, v85
	v_pk_fma_f32 v[2:3], v[70:71], v[4:5], v[2:3]
	v_mul_f32_e32 v4, 0xbfb8aa3b, v7
	v_exp_f32_e32 v4, v4
	v_rcp_f32_e32 v12, v12
	v_pk_mul_f32 v[2:3], v[2:3], v[6:7]
	s_waitcnt vmcnt(0)
	v_and_b32_e32 v5, 0xffff0000, v78
	v_add_f32_e32 v4, 1.0, v4
	v_rcp_f32_e32 v13, v4
	v_lshlrev_b32_e32 v4, 16, v78
	v_mul_f32_e32 v6, 0xbfb8aa3b, v4
	v_exp_f32_e32 v6, v6
	v_pk_mul_f32 v[82:83], v[2:3], v[12:13]
	v_add_f32_e32 v6, 1.0, v6
	v_pk_fma_f32 v[0:1], v[82:83], v[82:83], v[0:1]
	v_mul_f32_e32 v2, v83, v83
	v_pk_add_f32 v[0:1], v[2:3], v[0:1] op_sel_hi:[0,1]
	s_waitcnt lgkmcnt(0)
	v_lshlrev_b32_e32 v2, 16, v80
	v_and_b32_e32 v3, 0xffff0000, v80
	v_pk_fma_f32 v[2:3], v[70:71], v[2:3], v[8:9]
	v_rcp_f32_e32 v6, v6
	v_pk_mul_f32 v[2:3], v[2:3], v[4:5]
	v_mul_f32_e32 v4, 0xbfb8aa3b, v5
	v_exp_f32_e32 v4, v4
	v_and_b32_e32 v5, 0xffff0000, v79
	v_add_f32_e32 v4, 1.0, v4
	v_rcp_f32_e32 v7, v4
	v_lshlrev_b32_e32 v4, 16, v79
	v_pk_mul_f32 v[84:85], v[2:3], v[6:7]
	s_nop 0
	v_pk_fma_f32 v[0:1], v[84:85], v[84:85], v[0:1]
	v_mul_f32_e32 v2, v85, v85
	v_pk_add_f32 v[0:1], v[2:3], v[0:1] op_sel_hi:[0,1]
	v_lshlrev_b32_e32 v2, 16, v81
	v_and_b32_e32 v3, 0xffff0000, v81
	v_pk_fma_f32 v[2:3], v[70:71], v[2:3], v[10:11]
	v_mul_f32_e32 v6, 0xbfb8aa3b, v4
	v_pk_mul_f32 v[2:3], v[2:3], v[4:5]
	v_mul_f32_e32 v4, 0xbfb8aa3b, v5
	v_exp_f32_e32 v6, v6
	v_exp_f32_e32 v4, v4
	v_add_f32_e32 v6, 1.0, v6
	v_add_f32_e32 v4, 1.0, v4
	v_rcp_f32_e32 v6, v6
	v_rcp_f32_e32 v7, v4
	s_nop 0
	v_pk_mul_f32 v[70:71], v[2:3], v[6:7]
	s_nop 0
	v_pk_fma_f32 v[0:1], v[70:71], v[70:71], v[0:1]
	v_mul_f32_e32 v2, v71, v71
	v_pk_add_f32 v[0:1], v[2:3], v[0:1] op_sel_hi:[0,1]
	v_mov_b32_e32 v1, v0
	s_nop 1
	v_permlane16_swap_b32_e32 v0, v1
	v_add_f32_e32 v0, v0, v1
	v_mov_b32_e32 v1, v0
	s_nop 1
	v_permlane32_swap_b32_e32 v0, v1
	s_and_saveexec_b64 s[0:1], s[42:43]
	s_cbranch_execz .LBB0_1237
	v_add_f32_e32 v0, v0, v1
	ds_write_b32 v32, v0 offset:192
	s_branch .LBB0_1237
